# grid barrier: non-leader workgroups poll the top generation word directly (skip the per-XCD generation hop)
# baseline (speedup 1.0000x reference)
.LBB0_186:
	s_lshl_b32 s0, s57, 8
	s_add_u32 s23, s36, s0
	s_addc_u32 s22, s37, 0
	v_mov_b32_e32 v1, s23
	v_add_co_u32_e32 v6, vcc, 0x1000, v1
	v_mov_b32_e32 v1, s22
	s_nop 0
	v_addc_co_u32_e32 v7, vcc, 0, v1, vcc
	v_mov_b32_e32 v1, 1
	flat_atomic_add v1, v[6:7], v1 offset:1024 sc0
	v_cvt_f32_u32_e32 v3, v4
	v_sub_u32_e32 v5, 0, v4
	v_rcp_iflag_f32_e32 v3, v3
	s_nop 0
	v_mul_f32_e32 v3, 0x4f7ffffe, v3
	v_cvt_u32_f32_e32 v3, v3
	v_mul_lo_u32 v5, v5, v3
	v_mul_hi_u32 v5, v3, v5
	v_add_u32_e32 v3, v3, v5
	s_waitcnt vmcnt(0) lgkmcnt(0)
	v_mul_hi_u32 v3, v1, v3
	v_mul_lo_u32 v5, v3, v4
	v_add_u32_e32 v6, 1, v1
	v_sub_u32_e32 v1, v1, v5
	v_add_u32_e32 v7, 1, v3
	v_cmp_ge_u32_e32 vcc, v1, v4
	v_sub_u32_e32 v5, v1, v4
	s_nop 0
	v_cndmask_b32_e32 v3, v3, v7, vcc
	v_cndmask_b32_e32 v1, v1, v5, vcc
	v_add_u32_e32 v5, 1, v3
	v_cmp_ge_u32_e32 vcc, v1, v4
	s_nop 1
	v_cndmask_b32_e32 v1, v3, v5, vcc
	v_mad_u64_u32 v[4:5], s[0:1], v4, v1, v[4:5]
	v_cmp_ne_u32_e32 vcc, v6, v4
	s_and_saveexec_b64 s[0:1], vcc
	s_xor_b64 s[0:1], exec, s[0:1]
	s_cbranch_execz .LBB0_199
	v_mov_b32_e32 v2, s36
	v_add_co_u32_e32 v2, vcc, 0x3000, v2
	v_mov_b32_e32 v3, s37
	s_nop 0
	v_addc_co_u32_e32 v3, vcc, 0, v3, vcc
	flat_load_dword v2, v[2:3] offset:1280 sc1
	s_add_u32 s6, s36, 0x3500
	s_addc_u32 s7, s37, 0
	s_waitcnt vmcnt(0) lgkmcnt(0)
	v_cmp_eq_u32_e32 vcc, v2, v1
	s_and_saveexec_b64 s[4:5], vcc
	s_cbranch_execz .LBB0_198
	s_mov_b32 s24, 1
	s_mov_b64 s[8:9], 0
	s_branch .LBB0_190

.LBB0_279:
	s_lshl_b32 s0, s57, 8
	s_add_u32 s25, s36, s0
	s_addc_u32 s24, s37, 0
	v_mov_b32_e32 v1, s25
	v_add_co_u32_e32 v6, vcc, 0x1000, v1
	v_mov_b32_e32 v1, s24
	s_nop 0
	v_addc_co_u32_e32 v7, vcc, 0, v1, vcc
	v_mov_b32_e32 v1, 1
	flat_atomic_add v1, v[6:7], v1 offset:1024 sc0
	v_cvt_f32_u32_e32 v3, v4
	v_sub_u32_e32 v5, 0, v4
	v_rcp_iflag_f32_e32 v3, v3
	s_nop 0
	v_mul_f32_e32 v3, 0x4f7ffffe, v3
	v_cvt_u32_f32_e32 v3, v3
	v_mul_lo_u32 v5, v5, v3
	v_mul_hi_u32 v5, v3, v5
	v_add_u32_e32 v3, v3, v5
	s_waitcnt vmcnt(0) lgkmcnt(0)
	v_mul_hi_u32 v3, v1, v3
	v_mul_lo_u32 v5, v3, v4
	v_add_u32_e32 v6, 1, v1
	v_sub_u32_e32 v1, v1, v5
	v_add_u32_e32 v7, 1, v3
	v_cmp_ge_u32_e32 vcc, v1, v4
	v_sub_u32_e32 v5, v1, v4
	s_nop 0
	v_cndmask_b32_e32 v3, v3, v7, vcc
	v_cndmask_b32_e32 v1, v1, v5, vcc
	v_add_u32_e32 v5, 1, v3
	v_cmp_ge_u32_e32 vcc, v1, v4
	s_nop 1
	v_cndmask_b32_e32 v1, v3, v5, vcc
	v_mad_u64_u32 v[4:5], s[0:1], v4, v1, v[4:5]
	v_cmp_ne_u32_e32 vcc, v6, v4
	s_and_saveexec_b64 s[0:1], vcc
	s_xor_b64 s[0:1], exec, s[0:1]
	s_cbranch_execz .LBB0_292
	v_mov_b32_e32 v2, s36
	v_add_co_u32_e32 v2, vcc, 0x3000, v2
	v_mov_b32_e32 v3, s37
	s_nop 0
	v_addc_co_u32_e32 v3, vcc, 0, v3, vcc
	flat_load_dword v2, v[2:3] offset:1280 sc1
	s_add_u32 s8, s36, 0x3500
	s_addc_u32 s9, s37, 0
	s_waitcnt vmcnt(0) lgkmcnt(0)
	v_cmp_eq_u32_e32 vcc, v2, v1
	s_and_saveexec_b64 s[4:5], vcc
	s_cbranch_execz .LBB0_291
	s_mov_b32 s26, 1
	s_mov_b64 s[10:11], 0
	s_branch .LBB0_283

.LBB0_943:
	s_lshl_b32 s0, s80, 8
	s_add_u32 s25, s36, s0
	s_addc_u32 s24, s37, 0
	v_mov_b32_e32 v1, s25
	v_add_co_u32_e32 v6, vcc, 0x1000, v1
	v_mov_b32_e32 v1, s24
	s_nop 0
	v_addc_co_u32_e32 v7, vcc, 0, v1, vcc
	v_mov_b32_e32 v1, 1
	flat_atomic_add v3, v[6:7], v1 offset:1024 sc0
	v_cvt_f32_u32_e32 v1, v4
	v_sub_u32_e32 v5, 0, v4
	v_rcp_iflag_f32_e32 v1, v1
	s_nop 0
	v_mul_f32_e32 v1, 0x4f7ffffe, v1
	v_cvt_u32_f32_e32 v1, v1
	v_mul_lo_u32 v5, v5, v1
	v_mul_hi_u32 v5, v1, v5
	v_add_u32_e32 v1, v1, v5
	s_waitcnt vmcnt(0) lgkmcnt(0)
	v_mul_hi_u32 v1, v3, v1
	v_mul_lo_u32 v5, v1, v4
	v_sub_u32_e32 v5, v3, v5
	v_cmp_ge_u32_e32 vcc, v5, v4
	v_add_u32_e32 v6, 1, v1
	v_add_u32_e32 v3, 1, v3
	v_cndmask_b32_e32 v1, v1, v6, vcc
	v_sub_u32_e32 v6, v5, v4
	v_cndmask_b32_e32 v5, v5, v6, vcc
	v_cmp_ge_u32_e32 vcc, v5, v4
	v_add_u32_e32 v5, 1, v1
	s_nop 0
	v_cndmask_b32_e32 v1, v1, v5, vcc
	v_mad_u64_u32 v[4:5], s[0:1], v4, v1, v[4:5]
	v_cmp_ne_u32_e32 vcc, v3, v4
	s_and_saveexec_b64 s[0:1], vcc
	s_xor_b64 s[0:1], exec, s[0:1]
	s_cbranch_execz .LBB0_956
	v_mov_b32_e32 v2, s36
	v_add_co_u32_e32 v2, vcc, 0x3000, v2
	v_mov_b32_e32 v3, s37
	s_nop 0
	v_addc_co_u32_e32 v3, vcc, 0, v3, vcc
	flat_load_dword v2, v[2:3] offset:1280 sc1
	s_add_u32 s8, s36, 0x3500
	s_addc_u32 s9, s37, 0
	s_waitcnt vmcnt(0) lgkmcnt(0)
	v_cmp_eq_u32_e32 vcc, v2, v1
	s_and_saveexec_b64 s[4:5], vcc
	s_cbranch_execz .LBB0_955
	s_mov_b32 s26, 1
	s_mov_b64 s[10:11], 0
	s_branch .LBB0_947

.LBB0_1180:
	s_lshl_b32 s0, s80, 8
	s_add_u32 s27, s6, s0
	s_addc_u32 s26, s7, 0
	v_mov_b32_e32 v1, s27
	v_add_co_u32_e32 v6, vcc, 0x1000, v1
	v_mov_b32_e32 v1, s26
	s_nop 0
	v_addc_co_u32_e32 v7, vcc, 0, v1, vcc
	v_mov_b32_e32 v1, 1
	flat_atomic_add v3, v[6:7], v1 offset:1024 sc0
	v_cvt_f32_u32_e32 v1, v4
	v_sub_u32_e32 v5, 0, v4
	v_rcp_iflag_f32_e32 v1, v1
	s_nop 0
	v_mul_f32_e32 v1, 0x4f7ffffe, v1
	v_cvt_u32_f32_e32 v1, v1
	v_mul_lo_u32 v5, v5, v1
	v_mul_hi_u32 v5, v1, v5
	v_add_u32_e32 v1, v1, v5
	s_waitcnt vmcnt(0) lgkmcnt(0)
	v_mul_hi_u32 v1, v3, v1
	v_mul_lo_u32 v5, v1, v4
	v_sub_u32_e32 v5, v3, v5
	v_cmp_ge_u32_e32 vcc, v5, v4
	v_add_u32_e32 v6, 1, v1
	v_add_u32_e32 v3, 1, v3
	v_cndmask_b32_e32 v1, v1, v6, vcc
	v_sub_u32_e32 v6, v5, v4
	v_cndmask_b32_e32 v5, v5, v6, vcc
	v_cmp_ge_u32_e32 vcc, v5, v4
	v_add_u32_e32 v5, 1, v1
	s_nop 0
	v_cndmask_b32_e32 v1, v1, v5, vcc
	v_mad_u64_u32 v[4:5], s[0:1], v4, v1, v[4:5]
	v_cmp_ne_u32_e32 vcc, v3, v4
	s_and_saveexec_b64 s[0:1], vcc
	s_xor_b64 s[0:1], exec, s[0:1]
	s_cbranch_execz .LBB0_1193
	v_mov_b32_e32 v2, s6
	v_add_co_u32_e32 v2, vcc, 0x3000, v2
	v_mov_b32_e32 v3, s7
	s_nop 0
	v_addc_co_u32_e32 v3, vcc, 0, v3, vcc
	flat_load_dword v2, v[2:3] offset:1280 sc1
	s_add_u32 s10, s6, 0x3500
	s_addc_u32 s11, s7, 0
	s_waitcnt vmcnt(0) lgkmcnt(0)
	v_cmp_eq_u32_e32 vcc, v2, v1
	s_and_saveexec_b64 s[8:9], vcc
	s_cbranch_execz .LBB0_1192
	s_mov_b32 s28, 1
	s_mov_b64 s[12:13], 0
	s_branch .LBB0_1184

.LBB0_1727:
	s_lshl_b32 s0, s80, 8
	s_add_u32 s9, s6, s0
	s_addc_u32 s8, s7, 0
	v_mov_b32_e32 v1, s9
	v_add_co_u32_e32 v6, vcc, 0x1000, v1
	v_mov_b32_e32 v1, s8
	s_nop 0
	v_addc_co_u32_e32 v7, vcc, 0, v1, vcc
	v_mov_b32_e32 v1, 1
	flat_atomic_add v3, v[6:7], v1 offset:1024 sc0
	v_cvt_f32_u32_e32 v1, v4
	v_sub_u32_e32 v5, 0, v4
	v_rcp_iflag_f32_e32 v1, v1
	s_nop 0
	v_mul_f32_e32 v1, 0x4f7ffffe, v1
	v_cvt_u32_f32_e32 v1, v1
	v_mul_lo_u32 v5, v5, v1
	v_mul_hi_u32 v5, v1, v5
	v_add_u32_e32 v1, v1, v5
	s_waitcnt vmcnt(0) lgkmcnt(0)
	v_mul_hi_u32 v1, v3, v1
	v_mul_lo_u32 v5, v1, v4
	v_sub_u32_e32 v5, v3, v5
	v_cmp_ge_u32_e32 vcc, v5, v4
	v_add_u32_e32 v6, 1, v1
	v_add_u32_e32 v3, 1, v3
	v_cndmask_b32_e32 v1, v1, v6, vcc
	v_sub_u32_e32 v6, v5, v4
	v_cndmask_b32_e32 v5, v5, v6, vcc
	v_cmp_ge_u32_e32 vcc, v5, v4
	v_add_u32_e32 v5, 1, v1
	s_nop 0
	v_cndmask_b32_e32 v1, v1, v5, vcc
	v_mad_u64_u32 v[4:5], s[0:1], v4, v1, v[4:5]
	v_cmp_ne_u32_e32 vcc, v3, v4
	s_and_saveexec_b64 s[0:1], vcc
	s_xor_b64 s[0:1], exec, s[0:1]
	s_cbranch_execz .LBB0_1740
	v_mov_b32_e32 v2, s6
	v_add_co_u32_e32 v2, vcc, 0x3000, v2
	v_mov_b32_e32 v3, s7
	s_nop 0
	v_addc_co_u32_e32 v3, vcc, 0, v3, vcc
	flat_load_dword v2, v[2:3] offset:1280 sc1
	s_add_u32 s12, s6, 0x3500
	s_addc_u32 s13, s7, 0
	s_waitcnt vmcnt(0) lgkmcnt(0)
	v_cmp_eq_u32_e32 vcc, v2, v1
	s_and_saveexec_b64 s[10:11], vcc
	s_cbranch_execz .LBB0_1739
	s_mov_b32 s28, 1
	s_mov_b64 s[14:15], 0
	s_branch .LBB0_1731

.LBB0_1993:
	s_lshl_b32 s0, s80, 8
	s_add_u32 s9, s6, s0
	s_addc_u32 s8, s7, 0
	v_mov_b32_e32 v1, s9
	v_add_co_u32_e32 v6, vcc, 0x1000, v1
	v_mov_b32_e32 v1, s8
	s_nop 0
	v_addc_co_u32_e32 v7, vcc, 0, v1, vcc
	v_mov_b32_e32 v1, 1
	flat_atomic_add v3, v[6:7], v1 offset:1024 sc0
	v_cvt_f32_u32_e32 v1, v4
	v_sub_u32_e32 v5, 0, v4
	v_rcp_iflag_f32_e32 v1, v1
	s_nop 0
	v_mul_f32_e32 v1, 0x4f7ffffe, v1
	v_cvt_u32_f32_e32 v1, v1
	v_mul_lo_u32 v5, v5, v1
	v_mul_hi_u32 v5, v1, v5
	v_add_u32_e32 v1, v1, v5
	s_waitcnt vmcnt(0) lgkmcnt(0)
	v_mul_hi_u32 v1, v3, v1
	v_mul_lo_u32 v5, v1, v4
	v_sub_u32_e32 v5, v3, v5
	v_cmp_ge_u32_e32 vcc, v5, v4
	v_add_u32_e32 v6, 1, v1
	v_add_u32_e32 v3, 1, v3
	v_cndmask_b32_e32 v1, v1, v6, vcc
	v_sub_u32_e32 v6, v5, v4
	v_cndmask_b32_e32 v5, v5, v6, vcc
	v_cmp_ge_u32_e32 vcc, v5, v4
	v_add_u32_e32 v5, 1, v1
	s_nop 0
	v_cndmask_b32_e32 v1, v1, v5, vcc
	v_mad_u64_u32 v[4:5], s[0:1], v4, v1, v[4:5]
	v_cmp_ne_u32_e32 vcc, v3, v4
	s_and_saveexec_b64 s[0:1], vcc
	s_xor_b64 s[0:1], exec, s[0:1]
	s_cbranch_execz .LBB0_2006
	v_mov_b32_e32 v2, s6
	v_add_co_u32_e32 v2, vcc, 0x3000, v2
	v_mov_b32_e32 v3, s7
	s_nop 0
	v_addc_co_u32_e32 v3, vcc, 0, v3, vcc
	flat_load_dword v2, v[2:3] offset:1280 sc1
	s_add_u32 s14, s6, 0x3500
	s_addc_u32 s15, s7, 0
	s_waitcnt vmcnt(0) lgkmcnt(0)
	v_cmp_eq_u32_e32 vcc, v2, v1
	s_and_saveexec_b64 s[12:13], vcc
	s_cbranch_execz .LBB0_2005
	s_mov_b32 s10, 1
	s_mov_b64 s[16:17], 0
	s_branch .LBB0_1997

.LBB0_2597:
	s_lshl_b32 s0, s80, 8
	s_add_u32 s9, s88, s0
	s_addc_u32 s8, s89, 0
	v_mov_b32_e32 v1, s9
	v_add_co_u32_e32 v6, vcc, 0x1000, v1
	v_mov_b32_e32 v1, s8
	s_nop 0
	v_addc_co_u32_e32 v7, vcc, 0, v1, vcc
	v_mov_b32_e32 v1, 1
	flat_atomic_add v3, v[6:7], v1 offset:1024 sc0
	v_cvt_f32_u32_e32 v1, v4
	v_sub_u32_e32 v5, 0, v4
	v_rcp_iflag_f32_e32 v1, v1
	s_nop 0
	v_mul_f32_e32 v1, 0x4f7ffffe, v1
	v_cvt_u32_f32_e32 v1, v1
	v_mul_lo_u32 v5, v5, v1
	v_mul_hi_u32 v5, v1, v5
	v_add_u32_e32 v1, v1, v5
	s_waitcnt vmcnt(0) lgkmcnt(0)
	v_mul_hi_u32 v1, v3, v1
	v_mul_lo_u32 v5, v1, v4
	v_sub_u32_e32 v5, v3, v5
	v_cmp_ge_u32_e32 vcc, v5, v4
	v_add_u32_e32 v6, 1, v1
	v_add_u32_e32 v3, 1, v3
	v_cndmask_b32_e32 v1, v1, v6, vcc
	v_sub_u32_e32 v6, v5, v4
	v_cndmask_b32_e32 v5, v5, v6, vcc
	v_cmp_ge_u32_e32 vcc, v5, v4
	v_add_u32_e32 v5, 1, v1
	s_nop 0
	v_cndmask_b32_e32 v1, v1, v5, vcc
	v_mad_u64_u32 v[4:5], s[0:1], v4, v1, v[4:5]
	v_cmp_ne_u32_e32 vcc, v3, v4
	s_and_saveexec_b64 s[0:1], vcc
	s_xor_b64 s[0:1], exec, s[0:1]
	s_cbranch_execz .LBB0_2610
	v_mov_b32_e32 v2, s88
	v_add_co_u32_e32 v2, vcc, 0x3000, v2
	v_mov_b32_e32 v3, s89
	s_nop 0
	v_addc_co_u32_e32 v3, vcc, 0, v3, vcc
	flat_load_dword v2, v[2:3] offset:1280 sc1
	s_add_u32 s12, s88, 0x3500
	s_addc_u32 s13, s89, 0
	s_waitcnt vmcnt(0) lgkmcnt(0)
	v_cmp_eq_u32_e32 vcc, v2, v1
	s_and_saveexec_b64 s[6:7], vcc
	s_cbranch_execz .LBB0_2609
	s_mov_b32 s10, 1
	s_mov_b64 s[14:15], 0
	s_branch .LBB0_2601

.LBB0_3261:
	s_lshl_b32 s0, s79, 8
	s_add_u32 s9, s40, s0
	s_addc_u32 s8, s41, 0
	v_mov_b32_e32 v1, s9
	v_add_co_u32_e32 v6, vcc, 0x1000, v1
	v_mov_b32_e32 v1, s8
	s_nop 0
	v_addc_co_u32_e32 v7, vcc, 0, v1, vcc
	v_mov_b32_e32 v1, 1
	flat_atomic_add v1, v[6:7], v1 offset:1024 sc0
	v_cvt_f32_u32_e32 v3, v4
	v_sub_u32_e32 v5, 0, v4
	v_rcp_iflag_f32_e32 v3, v3
	s_nop 0
	v_mul_f32_e32 v3, 0x4f7ffffe, v3
	v_cvt_u32_f32_e32 v3, v3
	v_mul_lo_u32 v5, v5, v3
	v_mul_hi_u32 v5, v3, v5
	v_add_u32_e32 v3, v3, v5
	s_waitcnt vmcnt(0) lgkmcnt(0)
	v_mul_hi_u32 v3, v1, v3
	v_mul_lo_u32 v5, v3, v4
	v_add_u32_e32 v6, 1, v1
	v_sub_u32_e32 v1, v1, v5
	v_add_u32_e32 v7, 1, v3
	v_cmp_ge_u32_e32 vcc, v1, v4
	v_sub_u32_e32 v5, v1, v4
	s_nop 0
	v_cndmask_b32_e32 v3, v3, v7, vcc
	v_cndmask_b32_e32 v1, v1, v5, vcc
	v_add_u32_e32 v5, 1, v3
	v_cmp_ge_u32_e32 vcc, v1, v4
	s_nop 1
	v_cndmask_b32_e32 v1, v3, v5, vcc
	v_mad_u64_u32 v[4:5], s[0:1], v4, v1, v[4:5]
	v_cmp_ne_u32_e32 vcc, v6, v4
	s_and_saveexec_b64 s[0:1], vcc
	s_xor_b64 s[0:1], exec, s[0:1]
	s_cbranch_execz .LBB0_3274
	v_mov_b32_e32 v2, s40
	v_add_co_u32_e32 v2, vcc, 0x3000, v2
	v_mov_b32_e32 v3, s41
	s_nop 0
	v_addc_co_u32_e32 v3, vcc, 0, v3, vcc
	flat_load_dword v2, v[2:3] offset:1280 sc1
	s_add_u32 s12, s40, 0x3500
	s_addc_u32 s13, s41, 0
	s_waitcnt vmcnt(0) lgkmcnt(0)
	v_cmp_eq_u32_e32 vcc, v2, v1
	s_and_saveexec_b64 s[6:7], vcc
	s_cbranch_execz .LBB0_3273
	s_mov_b32 s10, 1
	s_mov_b64 s[14:15], 0
	s_branch .LBB0_3265

.LBB0_3885:
	s_lshl_b32 s0, s79, 8
	s_add_u32 s9, s40, s0
	s_addc_u32 s8, s41, 0
	v_mov_b32_e32 v1, s9
	v_add_co_u32_e32 v6, vcc, 0x1000, v1
	v_mov_b32_e32 v1, s8
	s_nop 0
	v_addc_co_u32_e32 v7, vcc, 0, v1, vcc
	v_mov_b32_e32 v1, 1
	flat_atomic_add v1, v[6:7], v1 offset:1024 sc0
	v_cvt_f32_u32_e32 v3, v4
	v_sub_u32_e32 v5, 0, v4
	v_rcp_iflag_f32_e32 v3, v3
	s_nop 0
	v_mul_f32_e32 v3, 0x4f7ffffe, v3
	v_cvt_u32_f32_e32 v3, v3
	v_mul_lo_u32 v5, v5, v3
	v_mul_hi_u32 v5, v3, v5
	v_add_u32_e32 v3, v3, v5
	s_waitcnt vmcnt(0) lgkmcnt(0)
	v_mul_hi_u32 v3, v1, v3
	v_mul_lo_u32 v5, v3, v4
	v_add_u32_e32 v6, 1, v1
	v_sub_u32_e32 v1, v1, v5
	v_add_u32_e32 v7, 1, v3
	v_cmp_ge_u32_e32 vcc, v1, v4
	v_sub_u32_e32 v5, v1, v4
	s_nop 0
	v_cndmask_b32_e32 v3, v3, v7, vcc
	v_cndmask_b32_e32 v1, v1, v5, vcc
	v_add_u32_e32 v5, 1, v3
	v_cmp_ge_u32_e32 vcc, v1, v4
	s_nop 1
	v_cndmask_b32_e32 v1, v3, v5, vcc
	v_mad_u64_u32 v[4:5], s[0:1], v4, v1, v[4:5]
	v_cmp_ne_u32_e32 vcc, v6, v4
	s_and_saveexec_b64 s[0:1], vcc
	s_xor_b64 s[0:1], exec, s[0:1]
	s_cbranch_execz .LBB0_3898
	v_mov_b32_e32 v2, s40
	v_add_co_u32_e32 v2, vcc, 0x3000, v2
	v_mov_b32_e32 v3, s41
	s_nop 0
	v_addc_co_u32_e32 v3, vcc, 0, v3, vcc
	flat_load_dword v2, v[2:3] offset:1280 sc1
	s_add_u32 s6, s40, 0x3500
	s_addc_u32 s7, s41, 0
	s_waitcnt vmcnt(0) lgkmcnt(0)
	v_cmp_eq_u32_e32 vcc, v2, v1
	s_and_saveexec_b64 s[4:5], vcc
	s_cbranch_execz .LBB0_3897
	s_mov_b32 s10, 1
	s_mov_b64 s[12:13], 0
	s_branch .LBB0_3889

.LBB0_4045:
	s_lshl_b32 s0, s79, 8
	s_add_u32 s11, s38, s0
	s_addc_u32 s10, s39, 0
	v_mov_b32_e32 v1, s11
	v_add_co_u32_e32 v6, vcc, 0x1000, v1
	v_mov_b32_e32 v1, s10
	s_nop 0
	v_addc_co_u32_e32 v7, vcc, 0, v1, vcc
	v_mov_b32_e32 v1, 1
	flat_atomic_add v1, v[6:7], v1 offset:1024 sc0
	v_cvt_f32_u32_e32 v3, v4
	v_sub_u32_e32 v5, 0, v4
	v_rcp_iflag_f32_e32 v3, v3
	s_nop 0
	v_mul_f32_e32 v3, 0x4f7ffffe, v3
	v_cvt_u32_f32_e32 v3, v3
	v_mul_lo_u32 v5, v5, v3
	v_mul_hi_u32 v5, v3, v5
	v_add_u32_e32 v3, v3, v5
	s_waitcnt vmcnt(0) lgkmcnt(0)
	v_mul_hi_u32 v3, v1, v3
	v_mul_lo_u32 v5, v3, v4
	v_add_u32_e32 v6, 1, v1
	v_sub_u32_e32 v1, v1, v5
	v_add_u32_e32 v7, 1, v3
	v_cmp_ge_u32_e32 vcc, v1, v4
	v_sub_u32_e32 v5, v1, v4
	s_nop 0
	v_cndmask_b32_e32 v3, v3, v7, vcc
	v_cndmask_b32_e32 v1, v1, v5, vcc
	v_add_u32_e32 v5, 1, v3
	v_cmp_ge_u32_e32 vcc, v1, v4
	s_nop 1
	v_cndmask_b32_e32 v1, v3, v5, vcc
	v_mad_u64_u32 v[4:5], s[0:1], v4, v1, v[4:5]
	v_cmp_ne_u32_e32 vcc, v6, v4
	s_and_saveexec_b64 s[0:1], vcc
	s_xor_b64 s[0:1], exec, s[0:1]
	s_cbranch_execz .LBB0_4058
	v_mov_b32_e32 v2, s38
	v_add_co_u32_e32 v2, vcc, 0x3000, v2
	v_mov_b32_e32 v3, s39
	s_nop 0
	v_addc_co_u32_e32 v3, vcc, 0, v3, vcc
	flat_load_dword v2, v[2:3] offset:1280 sc1
	s_add_u32 s6, s38, 0x3500
	s_addc_u32 s7, s39, 0
	s_waitcnt vmcnt(0) lgkmcnt(0)
	v_cmp_eq_u32_e32 vcc, v2, v1
	s_and_saveexec_b64 s[4:5], vcc
	s_cbranch_execz .LBB0_4057
	s_mov_b32 s24, 1
	s_mov_b64 s[8:9], 0
	s_branch .LBB0_4049

.LBB0_4280:
	s_lshl_b32 s0, s79, 8
	s_add_u32 s25, s36, s0
	s_addc_u32 s24, s37, 0
	v_mov_b32_e32 v1, s25
	v_add_co_u32_e32 v6, vcc, 0x1000, v1
	v_mov_b32_e32 v1, s24
	s_nop 0
	v_addc_co_u32_e32 v7, vcc, 0, v1, vcc
	v_mov_b32_e32 v1, 1
	flat_atomic_add v1, v[6:7], v1 offset:1024 sc0
	v_cvt_f32_u32_e32 v3, v4
	v_sub_u32_e32 v5, 0, v4
	v_rcp_iflag_f32_e32 v3, v3
	s_nop 0
	v_mul_f32_e32 v3, 0x4f7ffffe, v3
	v_cvt_u32_f32_e32 v3, v3
	v_mul_lo_u32 v5, v5, v3
	v_mul_hi_u32 v5, v3, v5
	v_add_u32_e32 v3, v3, v5
	s_waitcnt vmcnt(0) lgkmcnt(0)
	v_mul_hi_u32 v3, v1, v3
	v_mul_lo_u32 v5, v3, v4
	v_add_u32_e32 v6, 1, v1
	v_sub_u32_e32 v1, v1, v5
	v_add_u32_e32 v7, 1, v3
	v_cmp_ge_u32_e32 vcc, v1, v4
	v_sub_u32_e32 v5, v1, v4
	s_nop 0
	v_cndmask_b32_e32 v3, v3, v7, vcc
	v_cndmask_b32_e32 v1, v1, v5, vcc
	v_add_u32_e32 v5, 1, v3
	v_cmp_ge_u32_e32 vcc, v1, v4
	s_nop 1
	v_cndmask_b32_e32 v1, v3, v5, vcc
	v_mad_u64_u32 v[4:5], s[0:1], v4, v1, v[4:5]
	v_cmp_ne_u32_e32 vcc, v6, v4
	s_and_saveexec_b64 s[0:1], vcc
	s_xor_b64 s[0:1], exec, s[0:1]
	s_cbranch_execz .LBB0_4293
	v_mov_b32_e32 v2, s36
	v_add_co_u32_e32 v2, vcc, 0x3000, v2
	v_mov_b32_e32 v3, s37
	s_nop 0
	v_addc_co_u32_e32 v3, vcc, 0, v3, vcc
	flat_load_dword v2, v[2:3] offset:1280 sc1
	s_add_u32 s6, s36, 0x3500
	s_addc_u32 s7, s37, 0
	s_waitcnt vmcnt(0) lgkmcnt(0)
	v_cmp_eq_u32_e32 vcc, v2, v1
	s_and_saveexec_b64 s[4:5], vcc
	s_cbranch_execz .LBB0_4292
	s_mov_b32 s22, 1
	s_mov_b64 s[8:9], 0
	s_branch .LBB0_4284

.LBB0_4505:
	s_lshl_b32 s0, s79, 8
	s_add_u32 s23, s36, s0
	s_addc_u32 s22, s37, 0
	v_mov_b32_e32 v1, s23
	v_add_co_u32_e32 v6, vcc, 0x1000, v1
	v_mov_b32_e32 v1, s22
	s_nop 0
	v_addc_co_u32_e32 v7, vcc, 0, v1, vcc
	v_mov_b32_e32 v1, 1
	flat_atomic_add v1, v[6:7], v1 offset:1024 sc0
	v_cvt_f32_u32_e32 v3, v4
	v_sub_u32_e32 v5, 0, v4
	v_rcp_iflag_f32_e32 v3, v3
	s_nop 0
	v_mul_f32_e32 v3, 0x4f7ffffe, v3
	v_cvt_u32_f32_e32 v3, v3
	v_mul_lo_u32 v5, v5, v3
	v_mul_hi_u32 v5, v3, v5
	v_add_u32_e32 v3, v3, v5
	s_waitcnt vmcnt(0) lgkmcnt(0)
	v_mul_hi_u32 v3, v1, v3
	v_mul_lo_u32 v5, v3, v4
	v_add_u32_e32 v6, 1, v1
	v_sub_u32_e32 v1, v1, v5
	v_add_u32_e32 v7, 1, v3
	v_cmp_ge_u32_e32 vcc, v1, v4
	v_sub_u32_e32 v5, v1, v4
	s_nop 0
	v_cndmask_b32_e32 v3, v3, v7, vcc
	v_cndmask_b32_e32 v1, v1, v5, vcc
	v_add_u32_e32 v5, 1, v3
	v_cmp_ge_u32_e32 vcc, v1, v4
	s_nop 1
	v_cndmask_b32_e32 v1, v3, v5, vcc
	v_mad_u64_u32 v[4:5], s[0:1], v4, v1, v[4:5]
	v_cmp_ne_u32_e32 vcc, v6, v4
	s_and_saveexec_b64 s[0:1], vcc
	s_xor_b64 s[0:1], exec, s[0:1]
	s_cbranch_execz .LBB0_4518
	v_mov_b32_e32 v2, s36
	v_add_co_u32_e32 v2, vcc, 0x3000, v2
	v_mov_b32_e32 v3, s37
	s_nop 0
	v_addc_co_u32_e32 v3, vcc, 0, v3, vcc
	flat_load_dword v2, v[2:3] offset:1280 sc1
	s_add_u32 s6, s36, 0x3500
	s_addc_u32 s7, s37, 0
	s_waitcnt vmcnt(0) lgkmcnt(0)
	v_cmp_eq_u32_e32 vcc, v2, v1
	s_and_saveexec_b64 s[4:5], vcc
	s_cbranch_execz .LBB0_4517
	s_mov_b32 s24, 1
	s_mov_b64 s[8:9], 0
	s_branch .LBB0_4509

.LBB0_4581:
	s_lshl_b32 s0, s79, 8
	s_add_u32 s22, s82, s0
	s_addc_u32 s3, s83, 0
	v_mov_b32_e32 v1, s22
	v_add_co_u32_e32 v6, vcc, 0x1000, v1
	v_mov_b32_e32 v1, s3
	s_nop 0
	v_addc_co_u32_e32 v7, vcc, 0, v1, vcc
	v_mov_b32_e32 v1, 1
	flat_atomic_add v1, v[6:7], v1 offset:1024 sc0
	v_cvt_f32_u32_e32 v3, v4
	v_sub_u32_e32 v5, 0, v4
	v_rcp_iflag_f32_e32 v3, v3
	s_nop 0
	v_mul_f32_e32 v3, 0x4f7ffffe, v3
	v_cvt_u32_f32_e32 v3, v3
	v_mul_lo_u32 v5, v5, v3
	v_mul_hi_u32 v5, v3, v5
	v_add_u32_e32 v3, v3, v5
	s_waitcnt vmcnt(0) lgkmcnt(0)
	v_mul_hi_u32 v3, v1, v3
	v_mul_lo_u32 v5, v3, v4
	v_add_u32_e32 v6, 1, v1
	v_sub_u32_e32 v1, v1, v5
	v_add_u32_e32 v7, 1, v3
	v_cmp_ge_u32_e32 vcc, v1, v4
	v_sub_u32_e32 v5, v1, v4
	s_nop 0
	v_cndmask_b32_e32 v3, v3, v7, vcc
	v_cndmask_b32_e32 v1, v1, v5, vcc
	v_add_u32_e32 v5, 1, v3
	v_cmp_ge_u32_e32 vcc, v1, v4
	s_nop 1
	v_cndmask_b32_e32 v1, v3, v5, vcc
	v_mad_u64_u32 v[4:5], s[0:1], v4, v1, v[4:5]
	v_cmp_ne_u32_e32 vcc, v6, v4
	s_and_saveexec_b64 s[0:1], vcc
	s_xor_b64 s[0:1], exec, s[0:1]
	s_cbranch_execz .LBB0_4594
	v_mov_b32_e32 v2, s82
	v_add_co_u32_e32 v2, vcc, 0x3000, v2
	v_mov_b32_e32 v3, s83
	s_nop 0
	v_addc_co_u32_e32 v3, vcc, 0, v3, vcc
	flat_load_dword v2, v[2:3] offset:1280 sc1
	s_add_u32 s6, s82, 0x3500
	s_addc_u32 s7, s83, 0
	s_waitcnt vmcnt(0) lgkmcnt(0)
	v_cmp_eq_u32_e32 vcc, v2, v1
	s_and_saveexec_b64 s[4:5], vcc
	s_cbranch_execz .LBB0_4593
	s_mov_b32 s23, 1
	s_mov_b64 s[8:9], 0
	s_branch .LBB0_4585
